# session best plus convert_table without its L2 warm-up loads (next kernel by time share)
# baseline (speedup 1.0000x reference)
_Z13convert_tablePKfP15HIP_vector_typeIjLj4EEPKiS0_:
	v_mov_b32_e32 v1, 0
	s_mov_b64 s[4:5], exec
	s_branch .LBB0_8
	s_cmpk_gt_u32 s2, 0x3fff
	s_mov_b64 s[6:7], 0
	s_cbranch_scc1 .LBB0_3
	s_and_b32 s6, s2, 7
	s_lshr_b32 s3, s2, 3
	s_mulk_i32 s6, 0x103
	s_sub_i32 s8, s6, s3
	s_and_b32 s7, s2, 1
	s_addk_i32 s8, 0x102
	s_add_i32 s6, s6, s3
	s_cmp_eq_u32 s7, 0
	s_cselect_b32 s3, s6, s8
	s_and_b32 s6, s3, 0x7ff
